# P1->P2 barrier: first arriver of each XCD starts an L2 write-back early; longer spin caps for the P8 progress polls
# speedup vs baseline: 1.0100x; 1.0100x over previous
.LBB0_383:
	s_or_b64 exec, exec, s[2:3]
	v_cvt_f32_u32_e32 v6, v4
	s_waitcnt vmcnt(0)
	v_readfirstlane_b32 s2, v5
	v_sub_u32_e32 v5, 0, v4
	v_rcp_iflag_f32_e32 v6, v6
	v_add_u32_e32 v7, s2, v3
	v_mul_f32_e32 v6, 0x4f7ffffe, v6
	v_cvt_u32_f32_e32 v6, v6
	v_mul_lo_u32 v3, v5, v6
	v_mul_hi_u32 v3, v6, v3
	v_add_u32_e32 v3, v6, v3
	v_mul_hi_u32 v3, v7, v3
	v_mul_lo_u32 v5, v3, v4
	v_sub_u32_e32 v5, v7, v5
	v_add_u32_e32 v6, 1, v3
	v_cmp_ge_u32_e32 vcc, v5, v4
	s_nop 1
	v_cndmask_b32_e32 v3, v3, v6, vcc
	v_sub_u32_e32 v6, v5, v4
	v_cndmask_b32_e32 v5, v5, v6, vcc
	v_add_u32_e32 v6, 1, v3
	v_cmp_ge_u32_e32 vcc, v5, v4
	v_add_u32_e32 v5, 1, v7
	s_nop 0
	v_cndmask_b32_e32 v3, v3, v6, vcc
	v_mul_lo_u32 v6, v4, v3
	v_add_u32_e32 v4, v6, v4
	v_cmp_ne_u32_e32 vcc, v5, v4
	s_and_saveexec_b64 s[2:3], vcc
	s_xor_b64 s[2:3], exec, s[2:3]
	s_cbranch_execz .LBB0_397
	v_readlane_b32 s6, v255, 9
	s_waitcnt lgkmcnt(0)
	v_add_u32_e32 v2, 1, v6
	v_cmp_eq_u32_e32 vcc, v5, v2
	s_cbranch_vccz .Lfirstwb_1
	buffer_wbl2 sc1

.Lp8spin_f:
	global_load_dword v241, v240, s[28:29] sc1
	s_waitcnt vmcnt(0)
	v_cmp_le_u32_e32 vcc, s2, v241
	s_cmp_eq_u64 vcc, exec
	s_cbranch_scc1 .Lp8ready_f
	s_sleep 4
	s_add_u32 s5, s5, 1
	s_cmp_lt_u32 s5, 0x8000
	s_cbranch_scc1 .Lp8spin_f

.Lp8spin_n:
	global_load_dword v2, v0, s[28:29] sc1
	s_waitcnt vmcnt(0)
	v_cmp_le_u32_e32 vcc, s0, v2
	s_cmp_eq_u64 vcc, exec
	s_cbranch_scc1 .Lp8ready_n
	s_sleep 4
	s_add_u32 s3, s3, 1
	s_cmp_lt_u32 s3, 0x8000
	s_cbranch_scc1 .Lp8spin_n
